# speedup vs baseline: 1.0094x; 1.0094x over previous
_Z11attn_kernelPKDF16_S0_PDF16_:
	s_load_dwordx4 s[4:7], s[0:1], 0x0
	s_load_dwordx2 s[8:9], s[0:1], 0x10
	s_lshr_b32 s1, s2, 3
	s_lshr_b32 s10, s2, 7
	s_and_b32 s0, s2, 4
	s_and_b32 s1, s1, 8
	s_and_b32 s20, s2, 3
	s_lshl_b32 s30, s10, 4
	s_or_b32 s22, s1, s0
	s_or_b32 s0, s30, s20
	s_or_b32 s14, s0, s22
	s_or_b32 s0, s20, 16
	s_sub_i32 s0, s0, s30
	s_mov_b32 s15, 0
	s_or_b32 s0, s0, s22
	s_bfe_u32 s24, s2, 0x30003
	s_ashr_i32 s1, s0, 31
	s_lshl_b64 s[2:3], s[14:15], 18
	s_waitcnt lgkmcnt(0)
	s_add_u32 s2, s4, s2
	s_addc_u32 s3, s5, s3
	s_lshl_b64 s[0:1], s[0:1], 18
	s_add_u32 s11, s4, s0
	s_addc_u32 s12, s5, s1
	s_add_u32 s13, s6, s0
	v_readfirstlane_b32 s16, v0
	s_addc_u32 s18, s7, s1
	s_lshl_b32 s0, s24, 2
	s_lshr_b32 s1, s16, 7
	s_add_i32 s14, s1, s0
	s_lshr_b32 s23, s16, 6
	s_lshl_b64 s[0:1], s[14:15], 13
	s_add_u32 s0, s2, s0
	v_and_b32_e32 v189, 31, v0
	s_addc_u32 s1, s3, s1
	s_lshl_b32 s21, s23, 5
	v_and_or_b32 v1, s21, 32, v189
	v_lshlrev_b32_e32 v186, 4, v1
	v_mov_b32_e32 v187, 0
	s_lshl_b32 s14, s23, 9
	v_lshl_add_u64 v[2:3], s[0:1], 0, v[186:187]
	s_and_b32 s0, s16, 0x3fffffc0
	s_lshl_b64 s[16:17], s[14:15], 1
	v_and_b32_e32 v188, 63, v0
	s_add_u32 s2, s11, s16
	s_addc_u32 s3, s12, s17
	s_add_u32 s44, s2, 0x8000
	s_addc_u32 s45, s3, 0
	v_lshlrev_b32_e32 v186, 4, v188
	v_lshl_add_u64 v[44:45], s[2:3], 0, v[186:187]
	s_add_u32 s2, s13, s16
	s_addc_u32 s3, s18, s17
	s_add_u32 s46, s2, 0x6000
	s_addc_u32 s47, s3, 0
	s_lshl_b32 s25, s23, 10
	s_cmp_lg_u32 0, -1
	s_cselect_b32 s1, 0, 0
	v_bfe_u32 v46, v0, 5, 1
	s_add_i32 s25, s25, s1
	s_mov_b32 s1, m0
	s_mov_b32 m0, s25
	s_nop 0
	global_load_lds_dwordx4 v[44:45], off
	s_mov_b32 m0, s1
	v_lshl_add_u64 v[34:35], s[2:3], 0, v[186:187]
	s_add_i32 s26, s25, 0x6000
	v_lshlrev_b32_e32 v4, 10, v46
	s_mov_b32 s1, m0
	s_mov_b32 m0, s26
	s_nop 0
	global_load_lds_dwordx4 v[34:35], off
	s_mov_b32 m0, s1
	s_mov_b64 s[18:19], 0x2000
	v_mov_b32_e32 v5, v187
	v_lshl_add_u64 v[6:7], v[44:45], 0, s[18:19]
	s_add_i32 s1, s25, 0x2000
	s_mov_b32 s2, m0
	s_mov_b32 m0, s1
	s_nop 0
	global_load_lds_dwordx4 v[6:7], off
	s_mov_b32 m0, s2
	v_lshl_add_u64 v[2:3], v[2:3], 0, v[4:5]
	global_load_dwordx4 v[136:139], v[2:3], off
	global_load_dwordx4 v[128:131], v[2:3], off offset:2048
	s_movk_i32 s1, 0x1000
	v_add_co_u32_e32 v2, vcc, s1, v2
	v_lshlrev_b32_e32 v1, 4, v189
	s_nop 0
	v_addc_co_u32_e32 v3, vcc, 0, v3, vcc
	global_load_dwordx4 v[120:123], v[2:3], off
	global_load_dwordx4 v[112:115], v[2:3], off offset:2048
	v_add3_u32 v184, 0, v4, v1
	v_mov_b32_e32 v2, v187
	v_mov_b32_e32 v3, v187
	v_mov_b32_e32 v4, v187
	v_mov_b32_e32 v6, v187
	v_mov_b32_e32 v7, v187
	v_mov_b32_e32 v8, v187
	v_mov_b32_e32 v9, v187
	v_mov_b32_e32 v10, v187
	v_mov_b32_e32 v11, v187
	v_mov_b32_e32 v12, v187
	v_mov_b32_e32 v13, v187
	v_mov_b32_e32 v14, v187
	v_mov_b32_e32 v15, v187
	v_mov_b32_e32 v16, v187
	v_mov_b32_e32 v17, v187
	s_mov_b64 s[2:3], 0x4000
	v_lshl_add_u64 v[18:19], v[44:45], 0, s[2:3]
	s_add_i32 s1, s25, 0x4000
	s_mov_b32 s11, m0
	s_mov_b32 m0, s1
	s_nop 0
	global_load_lds_dwordx4 v[18:19], off
	s_mov_b32 m0, s11
	v_lshl_add_u64 v[18:19], v[34:35], 0, s[18:19]
	s_add_i32 s1, s25, 0x8000
	s_mov_b32 s11, m0
	s_mov_b32 m0, s1
	s_nop 0
	global_load_lds_dwordx4 v[18:19], off
	s_mov_b32 m0, s11
	s_waitcnt vmcnt(4) lgkmcnt(0)
	s_barrier
	ds_read_b128 v[36:39], v184
	ds_read_b128 v[40:43], v184 offset:512
	v_lshlrev_b32_e32 v190, 3, v0
	s_mov_b64 s[12:13], 0x6000
	s_or_b32 s14, s22, s20
	s_sub_i32 s14, s14, s30
	s_add_i32 s34, s14, 16
	s_lshl_b32 s0, s0, 2
	s_ashr_i32 s35, s34, 31
	s_lshl_b64 s[34:35], s[34:35], 18
	s_mov_b32 s27, -1
	s_waitcnt vmcnt(3) lgkmcnt(1)
	v_mfma_f32_32x32x16_f16 v[18:33], v[36:39], v[136:139], v[2:17]
	s_movk_i32 s28, 0x6000
	s_movk_i32 s31, 0x2000
	s_movk_i32 s29, 0x4000
	v_lshlrev_b32_e32 v191, 9, v46
	v_lshlrev_b32_e32 v182, 4, v46
	v_lshlrev_b32_e32 v180, 4, v188
	s_waitcnt lgkmcnt(0)
	v_mfma_f32_32x32x16_f16 v[2:17], v[40:43], v[136:139], v[2:17]
	ds_read_b128 v[36:39], v184 offset:2048
	ds_read_b128 v[40:43], v184 offset:2560
	s_waitcnt vmcnt(2) lgkmcnt(1)
	v_mfma_f32_32x32x16_f16 v[18:33], v[36:39], v[128:131], v[18:33]
	s_waitcnt lgkmcnt(0)
	v_mfma_f32_32x32x16_f16 v[2:17], v[40:43], v[128:131], v[2:17]
	ds_read_b128 v[36:39], v184 offset:4096
	ds_read_b128 v[40:43], v184 offset:4608
	s_waitcnt vmcnt(1) lgkmcnt(1)
	v_mfma_f32_32x32x16_f16 v[18:33], v[36:39], v[120:123], v[18:33]
	s_waitcnt lgkmcnt(0)
	v_mfma_f32_32x32x16_f16 v[2:17], v[40:43], v[120:123], v[2:17]
	ds_read_b128 v[36:39], v184 offset:6144
	ds_read_b128 v[40:43], v184 offset:6656
	s_waitcnt vmcnt(0) lgkmcnt(1)
	v_mfma_f32_32x32x16_f16 v[18:33], v[36:39], v[112:115], v[18:33]
	s_waitcnt lgkmcnt(0)
	v_mfma_f32_32x32x16_f16 v[2:17], v[40:43], v[112:115], v[2:17]
	s_nop 11
	v_max_f32_e32 v1, v19, v18
	v_max3_f32 v37, v20, v21, v3
	v_max3_f32 v1, v1, v2, v4
	v_max3_f32 v36, v37, v24, v25
	v_max3_f32 v1, v1, v5, v22
	v_max3_f32 v36, v36, v8, v9
	v_max3_f32 v1, v1, v23, v6
	v_max3_f32 v36, v36, v28, v29
	v_max3_f32 v1, v1, v7, v26
	v_max3_f32 v36, v36, v12, v13
	v_max3_f32 v1, v1, v27, v10
	v_max3_f32 v36, v36, v32, v33
	v_max3_f32 v1, v1, v11, v30
	v_max3_f32 v36, v36, v16, v17
	v_max3_f32 v1, v1, v31, v14
	v_max3_f32 v1, v1, v15, v36
	v_mov_b32_e32 v36, v1
	s_nop 1
	v_permlane32_swap_b32_e32 v1, v36
	v_max_f32_e32 v183, v36, v1
	v_lshlrev_b32_e32 v1, 1, v0
	v_sub_f32_e32 v36, v2, v183
	v_and_b32_e32 v1, 32, v1
	v_and_b32_e32 v2, 24, v190
	v_lshlrev_b32_e32 v0, 4, v0
	v_add3_u32 v1, 0, v1, v2
	v_and_b32_e32 v0, 0xc0, v0
	v_lshlrev_b32_e32 v2, 8, v46
	v_add3_u32 v181, v1, v2, v0
	v_xor_b32_e32 v0, 0x80000000, v183
	v_sub_f32_e32 v37, v3, v183
	v_sub_f32_e32 v38, v4, v183
	v_sub_f32_e32 v39, v5, v183
	v_sub_f32_e32 v40, v6, v183
	v_sub_f32_e32 v41, v7, v183
	v_sub_f32_e32 v42, v8, v183
	v_sub_f32_e32 v43, v9, v183
	v_sub_f32_e32 v47, v10, v183
	v_sub_f32_e32 v57, v11, v183
	v_sub_f32_e32 v58, v12, v183
	v_sub_f32_e32 v59, v13, v183
	v_sub_f32_e32 v60, v14, v183
	v_sub_f32_e32 v61, v15, v183
	v_mov_b32_e32 v1, v0
	v_mov_b32_e32 v2, v0
	v_mov_b32_e32 v3, v0
	v_mov_b32_e32 v4, v0
	v_mov_b32_e32 v5, v0
	v_mov_b32_e32 v6, v0
	v_mov_b32_e32 v7, v0
	v_mov_b32_e32 v8, v0
	v_mov_b32_e32 v9, v0
	v_mov_b32_e32 v10, v0
	v_mov_b32_e32 v11, v0
	v_mov_b32_e32 v12, v0
	v_mov_b32_e32 v13, v0
	v_mov_b32_e32 v14, v0
	v_mov_b32_e32 v15, v0
	s_waitcnt vmcnt(0) lgkmcnt(0)
	s_barrier
	v_sub_f32_e32 v62, v16, v183
	v_sub_f32_e32 v63, v17, v183
	v_lshl_add_u64 v[16:17], v[44:45], 0, s[12:13]
	s_mov_b32 s1, m0
	s_mov_b32 m0, s25
	s_nop 0
	global_load_lds_dwordx4 v[16:17], off
	s_mov_b32 m0, s1
	s_add_i32 s1, s25, 0xa000
	v_lshl_add_u64 v[16:17], v[34:35], 0, s[2:3]
	s_mov_b32 s11, m0
	s_mov_b32 m0, s1
	s_nop 0
	global_load_lds_dwordx4 v[16:17], off
	s_mov_b32 m0, s11
	ds_read_b128 v[172:175], v184 offset:8192
	ds_read_b128 v[168:171], v184 offset:8704
	ds_read_b128 v[164:167], v184 offset:10240
	ds_read_b128 v[160:163], v184 offset:10752
	ds_read_b128 v[156:159], v184 offset:12288
	ds_read_b128 v[152:155], v184 offset:12800
	ds_read_b128 v[148:151], v184 offset:14336
	ds_read_b128 v[144:147], v184 offset:14848
	s_add_i32 s11, s0, 0
	v_sub_f32_e32 v18, v18, v183
	v_sub_f32_e32 v19, v19, v183
	v_sub_f32_e32 v20, v20, v183
	v_sub_f32_e32 v21, v21, v183
	v_sub_f32_e32 v22, v22, v183
	v_sub_f32_e32 v23, v23, v183
	v_sub_f32_e32 v24, v24, v183
	v_sub_f32_e32 v25, v25, v183
	v_sub_f32_e32 v26, v26, v183
	v_sub_f32_e32 v27, v27, v183
	v_sub_f32_e32 v28, v28, v183
	v_sub_f32_e32 v29, v29, v183
	v_sub_f32_e32 v30, v30, v183
	v_sub_f32_e32 v31, v31, v183
	v_sub_f32_e32 v32, v32, v183
	v_sub_f32_e32 v33, v33, v183
	s_add_u32 s14, s16, s34
	v_exp_f32_e32 v64, v18
	v_exp_f32_e32 v65, v19
	v_exp_f32_e32 v48, v36
	v_exp_f32_e32 v49, v37
	v_exp_f32_e32 v66, v20
	v_exp_f32_e32 v50, v38
	v_exp_f32_e32 v67, v21
	v_exp_f32_e32 v51, v39
	v_exp_f32_e32 v68, v22
	v_exp_f32_e32 v52, v40
	v_exp_f32_e32 v69, v23
	v_exp_f32_e32 v53, v41
	v_exp_f32_e32 v70, v24
	v_exp_f32_e32 v54, v42
	v_exp_f32_e32 v71, v25
	v_exp_f32_e32 v55, v43
	v_exp_f32_e32 v72, v26
	v_exp_f32_e32 v56, v47
	v_exp_f32_e32 v73, v27
	v_exp_f32_e32 v57, v57
	v_exp_f32_e32 v74, v28
	v_exp_f32_e32 v58, v58
	v_exp_f32_e32 v75, v29
	v_exp_f32_e32 v59, v59
	v_exp_f32_e32 v76, v30
	v_exp_f32_e32 v60, v60
	v_exp_f32_e32 v77, v31
	v_exp_f32_e32 v61, v61
	v_exp_f32_e32 v78, v32
	v_exp_f32_e32 v62, v62
	v_exp_f32_e32 v79, v33
	v_exp_f32_e32 v63, v63
	s_addc_u32 s16, s17, s35
	s_waitcnt vmcnt(2) lgkmcnt(0)
	s_barrier
	v_or_b32_e32 v16, s14, v186
	v_mov_b32_e32 v17, s16
	v_lshl_add_u64 v[16:17], v[16:17], 0, s[18:19]
	v_cmp_gt_u32_e64 s[0:1], 32, v188
	s_mov_b32 s16, 0x41000000
	s_mov_b32 s36, 0x43800000
	s_mov_b64 s[4:5], 0x8000
	s_movk_i32 s14, 0x2000
	s_movk_i32 s19, 0x4000
	v_mov_b32_e32 v16, v187
	v_mov_b32_e32 v17, v187
	v_mov_b32_e32 v18, v187
	v_mov_b32_e32 v19, v187
	v_mov_b32_e32 v20, v187
	v_mov_b32_e32 v21, v187
	v_mov_b32_e32 v22, v187
	v_mov_b32_e32 v23, v187
	v_mov_b32_e32 v24, v187
	v_mov_b32_e32 v25, v187
	v_mov_b32_e32 v26, v187
	v_mov_b32_e32 v27, v187
	v_mov_b32_e32 v28, v187
	v_mov_b32_e32 v29, v187
	v_mov_b32_e32 v30, v187
	v_mov_b32_e32 v31, v187
	v_mov_b32_e32 v32, v187
	v_mov_b32_e32 v33, v187
	v_mov_b32_e32 v34, v187
	v_mov_b32_e32 v35, v187
	v_mov_b32_e32 v36, v187
	v_mov_b32_e32 v37, v187
	v_mov_b32_e32 v38, v187
	v_mov_b32_e32 v39, v187
	v_mov_b32_e32 v40, v187
	v_mov_b32_e32 v41, v187
	v_mov_b32_e32 v42, v187
	v_mov_b32_e32 v43, v187
	v_mov_b32_e32 v44, v187
	v_mov_b32_e32 v45, v187
	v_mov_b32_e32 v46, v187
	v_mov_b32_e32 v47, v187
	v_lshl_add_u32 v186, v189, 2, s11
	s_nop 0
	s_nop 0
	s_nop 0
	s_nop 0
